# MLA loop: second-group PV fragment reads moved into the QK gaps (shorter QK-to-PV transition)
# baseline (speedup 1.0000x reference)
; __device__ __forceinline__ void finishSM(f32x16& p0, f32x16& p1, float alpha, float& l_reg, bf16x8& pa0, bf16x8& pa1, bf16x8& pa2, bf16x8& pa3) {
; #pragma unroll
;     for (int r = 0; r < 16; ++r) p1[r] = EXP_PROBE ? fmaf(p1[r], 0.001f, 1.f) : __builtin_amdgcn_exp2f(p1[r]);
;     float ps = 0.f;
; #pragma unroll
;     for (int r = 0; r < 16; ++r) ps += p0[r];
; #pragma unroll
;     for (int r = 0; r < 16; ++r) ps += p1[r];
;     { auto rr = __builtin_amdgcn_permlane32_swap(__float_as_uint(ps), __float_as_uint(ps), false, false);
;       ps = __uint_as_float(rr[0]) + __uint_as_float(rr[1]); }
;     l_reg = l_reg * alpha + ps;
;     ATT_PKN(p0, 0, pa0); ATT_PKN(p0, 8, pa1); ATT_PKN(p1, 0, pa2); ATT_PKN(p1, 8, pa3);
; }
; template <int DQK> __device__ __forceinline__ void qkt(f32x16& p0, f32x16& p1, const LAS char* buf, const bf16x8* qr, int r32, int hi, const f32x16& negm) {
; #pragma unroll
;     for (int d0 = 0; d0 < 4; ++d0) { const int ch = d0 * 2 + hi;
;         const bf16x8 b0 = *(const LAS bf16x8*)(buf + B_KN + swz64(r32, ch));
;         const bf16x8 b1 = *(const LAS bf16x8*)(buf + B_KN + swz64(32 + r32, ch));
;         p0 = __builtin_amdgcn_mfma_f32_32x32x16_bf16(b0, qr[d0], d0 == 0 ? negm : p0, 0, 0, 0);
;         p1 = __builtin_amdgcn_mfma_f32_32x32x16_bf16(b1, qr[d0], d0 == 0 ? negm : p1, 0, 0, 0); }
;     if constexpr (DQK == 96) {
; #pragma unroll
;         for (int d0 = 0; d0 < 2; ++d0) { const int ch = d0 * 2 + hi;
;             const bf16x8 b0 = *(const LAS bf16x8*)(buf + B_KR + swz32(r32, ch));
;             const bf16x8 b1 = *(const LAS bf16x8*)(buf + B_KR + swz32(32 + r32, ch));
;             p0 = __builtin_amdgcn_mfma_f32_32x32x16_bf16(b0, qr[4 + d0], p0, 0, 0, 0);
;             p1 = __builtin_amdgcn_mfma_f32_32x32x16_bf16(b1, qr[4 + d0], p1, 0, 0, 0); }
;     }
; }
; template <int D0> __device__ __forceinline__ void pv_one(f32x16& od, unsigned vb, bf16x8 pa0, bf16x8 pa1, bf16x8 pa2, bf16x8 pa3) {
;     const s16x4 l0 = tr_read<v_rd_off(D0, 0, 0)>(vb), h0 = tr_read<v_rd_off(D0, 0, 1)>(vb), l1 = tr_read<v_rd_off(D0, 1, 0)>(vb), h1 = tr_read<v_rd_off(D0, 1, 1)>(vb);
;     const s16x4 l2 = tr_read<v_rd_off(D0, 2, 0)>(vb), h2 = tr_read<v_rd_off(D0, 2, 1)>(vb), l3 = tr_read<v_rd_off(D0, 3, 0)>(vb), h3 = tr_read<v_rd_off(D0, 3, 1)>(vb);
;     asm volatile("s_waitcnt lgkmcnt(0)" ::: "memory"); SBAR();
.LBB0_523:
	s_mov_b32 s10, s0
	s_waitcnt lgkmcnt(0)
	s_barrier
	v_add_u32_e32 v2, s13, v201
	v_add_u32_e32 v8, v2, v209
	ds_read_b128 v[4:7], v8
	ds_read_b128 v[8:11], v8 offset:4096
	v_add_u32_e32 v246, v2, v210
	ds_read_b128 v[174:177], v246
	ds_read_b128 v[246:249], v246 offset:4096
	v_add_u32_e32 v78, v2, v211
	ds_read_b128 v[250:253], v78
	ds_read_b128 v[78:81], v78 offset:4096
	v_add_u32_e32 v16, v2, v212
	ds_read_b128 v[12:15], v16
	v_add_u32_e32 v2, s13, v217
	v_exp_f32_e32 v98, v98
	v_exp_f32_e32 v99, v99
	v_exp_f32_e32 v100, v100
	v_exp_f32_e32 v101, v101
	v_exp_f32_e32 v102, v102
	v_exp_f32_e32 v103, v103
	v_exp_f32_e32 v104, v104
	v_exp_f32_e32 v105, v105
	s_waitcnt lgkmcnt(6)
	v_mfma_f32_32x32x16_bf16 v[130:145], v[4:7], v[166:169], v[82:97]
	ds_read_b128 v[4:7], v16 offset:4096
	v_exp_f32_e32 v106, v106
	v_exp_f32_e32 v107, v107
	v_exp_f32_e32 v108, v108
	v_cvt_pk_bf16_f32 v74, v243, v245
	s_waitcnt lgkmcnt(6)
	v_mfma_f32_32x32x16_bf16 v[114:129], v[8:11], v[166:169], v[82:97]
	v_add_u32_e32 v16, v2, v219
	ds_read_b128 v[8:11], v16 offset:8192
	v_exp_f32_e32 v109, v109
	v_exp_f32_e32 v110, v110
	v_exp_f32_e32 v111, v111
	v_cvt_pk_bf16_f32 v75, v241, v244
	s_waitcnt lgkmcnt(6)
	v_mfma_f32_32x32x16_bf16 v[130:145], v[174:177], v[162:165], v[130:145]
	ds_read_b128 v[174:177], v16 offset:10240
	v_exp_f32_e32 v112, v112
	v_exp_f32_e32 v113, v113
	v_cvt_pk_bf16_f32 v76, v239, v242
	v_cvt_pk_bf16_f32 v77, v238, v240
	v_add_f32_e32 v229, 0, v243
	v_add_f32_e32 v229, v245, v229
	s_waitcnt lgkmcnt(6)
	v_mfma_f32_32x32x16_bf16 v[114:129], v[246:249], v[162:165], v[114:129]
	v_add_u32_e32 v16, v2, v220
	ds_read_b128 v[246:249], v16 offset:8192
	v_cvt_pk_bf16_f32 v66, v236, v237
	v_cvt_pk_bf16_f32 v67, v233, v235
	v_add_f32_e32 v229, v241, v229
	v_add_f32_e32 v229, v244, v229
	v_add_f32_e32 v229, v239, v229
	v_add_f32_e32 v229, v242, v229
	s_waitcnt lgkmcnt(6)
	v_mfma_f32_32x32x16_bf16 v[130:145], v[250:253], v[158:161], v[130:145]
	ds_read_b128 v[250:253], v16 offset:10240
	v_cvt_pk_bf16_f32 v68, v231, v234
	v_cvt_pk_bf16_f32 v69, v230, v232
	v_add_f32_e32 v229, v238, v229
	v_add_f32_e32 v229, v240, v229
	v_add_f32_e32 v229, v236, v229
	v_add_f32_e32 v229, v237, v229
	s_waitcnt lgkmcnt(6)
	v_mfma_f32_32x32x16_bf16 v[114:129], v[78:81], v[158:161], v[114:129]
	v_add_f32_e32 v229, v233, v229
	v_add_f32_e32 v229, v235, v229
	v_add_f32_e32 v229, v231, v229
	v_add_f32_e32 v229, v234, v229
	v_add_f32_e32 v229, v230, v229
	v_add_f32_e32 v229, v232, v229
	s_waitcnt lgkmcnt(5)
	v_mfma_f32_32x32x16_bf16 v[130:145], v[12:15], v[154:157], v[130:145]
	v_add_u32_e32 v17, s11, v213
	ds_read_b64_tr_b16 v[230:231], v17 offset:0
	ds_read_b64_tr_b16 v[232:233], v17 offset:1024
	ds_read_b64_tr_b16 v[234:235], v17 offset:2048
	ds_read_b64_tr_b16 v[236:237], v17 offset:3072
	v_add_f32_e32 v229, v98, v229
	v_add_f32_e32 v229, v99, v229
	v_add_f32_e32 v229, v100, v229
	v_add_f32_e32 v229, v101, v229
	s_waitcnt lgkmcnt(8)
	v_mfma_f32_32x32x16_bf16 v[114:129], v[4:7], v[154:157], v[114:129]
	ds_read_b64_tr_b16 v[238:239], v17 offset:4096
	ds_read_b64_tr_b16 v[240:241], v17 offset:5120
	ds_read_b64_tr_b16 v[242:243], v17 offset:6144
	ds_read_b64_tr_b16 v[244:245], v17 offset:7168
	v_add_f32_e32 v229, v102, v229
	v_add_f32_e32 v229, v103, v229
	v_add_f32_e32 v229, v104, v229
	v_add_f32_e32 v229, v105, v229
	s_waitcnt lgkmcnt(11)
	v_mfma_f32_32x32x16_bf16 v[130:145], v[8:11], v[150:153], v[130:145]
	v_add_f32_e32 v229, v106, v229
	v_add_f32_e32 v229, v107, v229
	v_add_f32_e32 v229, v108, v229
	v_add_f32_e32 v229, v109, v229
	v_add_f32_e32 v229, v110, v229
	v_add_f32_e32 v229, v111, v229
	ds_read_b64_tr_b16 v[78:79], v17 offset:512
	ds_read_b64_tr_b16 v[80:81], v17 offset:1536
	s_waitcnt lgkmcnt(12)
	v_mfma_f32_32x32x16_bf16 v[114:129], v[174:177], v[150:153], v[114:129]
	v_add_f32_e32 v229, v112, v229
	v_add_f32_e32 v228, v113, v229
	v_mov_b32_e32 v229, v228
	v_cvt_pk_bf16_f32 v70, v98, v99
	v_cvt_pk_bf16_f32 v71, v100, v101
	v_cvt_pk_bf16_f32 v72, v102, v103
	v_cvt_pk_bf16_f32 v73, v104, v105
	v_cvt_pk_bf16_f32 v12, v106, v107
	v_cvt_pk_bf16_f32 v13, v108, v109
	v_cvt_pk_bf16_f32 v14, v110, v111
	v_cvt_pk_bf16_f32 v15, v112, v113
	v_permlane32_swap_b32_e32 v228, v229
	s_waitcnt lgkmcnt(11)
	v_mfma_f32_32x32x16_bf16 v[130:145], v[246:249], v[146:149], v[130:145]
	s_add_i32 s36, s35, -1
	s_cmp_lt_u32 s36, s30
	s_cselect_b32 s0, 0, s30
	s_cselect_b32 s1, s29, s34
	s_lshl_b32 s0, s0, 6
	s_sub_i32 s37, s1, s0
	s_lshl_b32 s1, s36, 6
	s_add_i32 s37, s37, s1
	s_lshl_b32 s0, s37, 6
	s_add_u32 s48, s44, s0
	s_addc_u32 s49, s45, 0
	s_lshl_b32 s0, s37, 11
	s_add_u32 s46, s42, s0
	s_addc_u32 s47, s43, 0
	global_load_dwordx4 v[174:177], v226, s[48:49]
	ds_read_b64_tr_b16 v[98:99], v17 offset:2560
	ds_read_b64_tr_b16 v[100:101], v17 offset:3584
	ds_read_b64_tr_b16 v[102:103], v17 offset:4608
	s_waitcnt lgkmcnt(13)
	v_mfma_f32_32x32x16_bf16 v[114:129], v[250:253], v[146:149], v[114:129]
	global_load_dwordx4 v[8:11], v225, s[46:47]
	global_load_dwordx4 v[4:7], v225, s[46:47] offset:128
	ds_read_b64_tr_b16 v[104:105], v17 offset:5632
	ds_read_b64_tr_b16 v[110:111], v17 offset:6656
	ds_read_b64_tr_b16 v[112:113], v17 offset:7680
	s_nop 3
	v_max3_f32 v2, v130, v131, v132
	v_max3_f32 v2, v2, v133, v134
	v_max3_f32 v2, v2, v135, v136
	v_max3_f32 v2, v2, v137, v138
	v_max3_f32 v2, v2, v139, v140
	v_max3_f32 v2, v2, v141, v142
	v_max3_f32 v2, v2, v143, v144
	v_max3_f32 v2, v2, v145, v114
	v_max3_f32 v2, v2, v115, v116
	s_waitcnt lgkmcnt(8)
	v_mfma_f32_32x32x16_bf16 v[50:65], v[230:233], v[74:77], v[50:65]
	v_max3_f32 v2, v2, v117, v118
	v_max3_f32 v2, v2, v119, v120
	v_max3_f32 v2, v2, v121, v122
	v_mfma_f32_32x32x16_bf16 v[50:65], v[234:237], v[66:69], v[50:65]
	v_max3_f32 v2, v2, v123, v124
	v_max3_f32 v2, v2, v125, v126
	v_max3_f32 v2, v2, v127, v128
	v_mfma_f32_32x32x16_bf16 v[50:65], v[238:241], v[70:73], v[50:65]
	v_max_f32_e32 v2, v2, v129
	s_nop 0
	s_nop 0
	v_mfma_f32_32x32x16_bf16 v[50:65], v[242:245], v[12:15], v[50:65]
	v_mov_b32_e32 v16, v2
	s_nop 1
	v_permlane32_swap_b32_e32 v2, v16
	v_max_f32_e32 v2, v2, v16
	v_cmp_ge_f32_e32 vcc, s28, v2
	s_cmp_eq_u64 vcc, exec
	s_cbranch_scc0 .LBB0_542
	v_mov_b32_e32 v2, 1.0

; __device__ __forceinline__ void finishSM(f32x16& p0, f32x16& p1, float alpha, float& l_reg, bf16x8& pa0, bf16x8& pa1, bf16x8& pa2, bf16x8& pa3) {
; #pragma unroll
;     for (int r = 0; r < 16; ++r) p1[r] = EXP_PROBE ? fmaf(p1[r], 0.001f, 1.f) : __builtin_amdgcn_exp2f(p1[r]);
;     float ps = 0.f;
; #pragma unroll
;     for (int r = 0; r < 16; ++r) ps += p0[r];
; #pragma unroll
;     for (int r = 0; r < 16; ++r) ps += p1[r];
;     { auto rr = __builtin_amdgcn_permlane32_swap(__float_as_uint(ps), __float_as_uint(ps), false, false);
;       ps = __uint_as_float(rr[0]) + __uint_as_float(rr[1]); }
;     l_reg = l_reg * alpha + ps;
;     ATT_PKN(p0, 0, pa0); ATT_PKN(p0, 8, pa1); ATT_PKN(p1, 0, pa2); ATT_PKN(p1, 8, pa3);
; }
; template <int DQK> __device__ __forceinline__ void qkt(f32x16& p0, f32x16& p1, const LAS char* buf, const bf16x8* qr, int r32, int hi, const f32x16& negm) {
; #pragma unroll
;     for (int d0 = 0; d0 < 4; ++d0) { const int ch = d0 * 2 + hi;
;         const bf16x8 b0 = *(const LAS bf16x8*)(buf + B_KN + swz64(r32, ch));
;         const bf16x8 b1 = *(const LAS bf16x8*)(buf + B_KN + swz64(32 + r32, ch));
;         p0 = __builtin_amdgcn_mfma_f32_32x32x16_bf16(b0, qr[d0], d0 == 0 ? negm : p0, 0, 0, 0);
;         p1 = __builtin_amdgcn_mfma_f32_32x32x16_bf16(b1, qr[d0], d0 == 0 ? negm : p1, 0, 0, 0); }
;     if constexpr (DQK == 96) {
; #pragma unroll
;         for (int d0 = 0; d0 < 2; ++d0) { const int ch = d0 * 2 + hi;
;             const bf16x8 b0 = *(const LAS bf16x8*)(buf + B_KR + swz32(r32, ch));
;             const bf16x8 b1 = *(const LAS bf16x8*)(buf + B_KR + swz32(32 + r32, ch));
;             p0 = __builtin_amdgcn_mfma_f32_32x32x16_bf16(b0, qr[4 + d0], p0, 0, 0, 0);
;             p1 = __builtin_amdgcn_mfma_f32_32x32x16_bf16(b1, qr[4 + d0], p1, 0, 0, 0); }
;     }
; }
; template <int D0> __device__ __forceinline__ void pv_one(f32x16& od, unsigned vb, bf16x8 pa0, bf16x8 pa1, bf16x8 pa2, bf16x8 pa3) {
;     const s16x4 l0 = tr_read<v_rd_off(D0, 0, 0)>(vb), h0 = tr_read<v_rd_off(D0, 0, 1)>(vb), l1 = tr_read<v_rd_off(D0, 1, 0)>(vb), h1 = tr_read<v_rd_off(D0, 1, 1)>(vb);
;     const s16x4 l2 = tr_read<v_rd_off(D0, 2, 0)>(vb), h2 = tr_read<v_rd_off(D0, 2, 1)>(vb), l3 = tr_read<v_rd_off(D0, 3, 0)>(vb), h3 = tr_read<v_rd_off(D0, 3, 1)>(vb);
;     asm volatile("s_waitcnt lgkmcnt(0)" ::: "memory"); SBAR();
.LBB0_531:
	s_waitcnt lgkmcnt(0)
	s_barrier
	v_add_u32_e32 v17, s10, v201
	v_add_u32_e32 v182, v17, v209
	ds_read_b128 v[178:181], v182
	ds_read_b128 v[182:185], v182 offset:4096
	v_add_u32_e32 v66, v17, v210
	ds_read_b128 v[170:173], v66
	ds_read_b128 v[66:69], v66 offset:4096
	v_add_u32_e32 v74, v17, v211
	ds_read_b128 v[70:73], v74
	ds_read_b128 v[74:77], v74 offset:4096
	v_add_u32_e32 v253, v17, v212
	ds_read_b128 v[78:81], v253
	v_add_u32_e32 v17, s10, v217
	v_exp_f32_e32 v114, v114
	v_exp_f32_e32 v115, v115
	v_exp_f32_e32 v116, v116
	v_exp_f32_e32 v117, v117
	v_exp_f32_e32 v118, v118
	v_exp_f32_e32 v119, v119
	v_exp_f32_e32 v120, v120
	v_exp_f32_e32 v121, v121
	s_waitcnt lgkmcnt(6)
	v_mfma_f32_32x32x16_bf16 v[130:145], v[178:181], v[166:169], v[82:97]
	ds_read_b128 v[178:181], v253 offset:4096
	v_exp_f32_e32 v122, v122
	v_exp_f32_e32 v123, v123
	v_exp_f32_e32 v124, v124
	v_cvt_pk_bf16_f32 v12, v16, v234
	s_waitcnt lgkmcnt(6)
	v_mfma_f32_32x32x16_bf16 v[98:113], v[182:185], v[166:169], v[82:97]
	v_add_u32_e32 v253, v17, v219
	ds_read_b128 v[182:185], v253 offset:8192
	v_exp_f32_e32 v125, v125
	v_exp_f32_e32 v126, v126
	v_exp_f32_e32 v127, v127
	v_cvt_pk_bf16_f32 v13, v235, v236
	s_waitcnt lgkmcnt(6)
	v_mfma_f32_32x32x16_bf16 v[130:145], v[170:173], v[162:165], v[130:145]
	ds_read_b128 v[170:173], v253 offset:10240
	v_exp_f32_e32 v128, v128
	v_exp_f32_e32 v129, v129
	v_cvt_pk_bf16_f32 v14, v237, v238
	v_cvt_pk_bf16_f32 v15, v239, v240
	v_add_f32_e32 v252, 0, v16
	v_add_f32_e32 v252, v234, v252
	s_waitcnt lgkmcnt(6)
	v_mfma_f32_32x32x16_bf16 v[98:113], v[66:69], v[162:165], v[98:113]
	v_add_u32_e32 v253, v17, v220
	ds_read_b128 v[66:69], v253 offset:8192
	v_cvt_pk_bf16_f32 v230, v241, v242
	v_cvt_pk_bf16_f32 v231, v243, v244
	v_add_f32_e32 v252, v235, v252
	v_add_f32_e32 v252, v236, v252
	v_add_f32_e32 v252, v237, v252
	v_add_f32_e32 v252, v238, v252
	s_waitcnt lgkmcnt(6)
	v_mfma_f32_32x32x16_bf16 v[130:145], v[70:73], v[158:161], v[130:145]
	ds_read_b128 v[70:73], v253 offset:10240
	v_cvt_pk_bf16_f32 v232, v245, v246
	v_cvt_pk_bf16_f32 v233, v247, v248
	v_add_f32_e32 v252, v239, v252
	v_add_f32_e32 v252, v240, v252
	v_add_f32_e32 v252, v241, v252
	v_add_f32_e32 v252, v242, v252
	s_waitcnt lgkmcnt(6)
	v_mfma_f32_32x32x16_bf16 v[98:113], v[74:77], v[158:161], v[98:113]
	v_add_f32_e32 v252, v243, v252
	v_add_f32_e32 v252, v244, v252
	v_add_f32_e32 v252, v245, v252
	v_add_f32_e32 v252, v246, v252
	v_add_f32_e32 v252, v247, v252
	v_add_f32_e32 v252, v248, v252
	s_waitcnt lgkmcnt(5)
	v_mfma_f32_32x32x16_bf16 v[130:145], v[78:81], v[154:157], v[130:145]
	v_add_u32_e32 v16, s13, v213
	ds_read_b64_tr_b16 v[234:235], v16 offset:0
	ds_read_b64_tr_b16 v[236:237], v16 offset:1024
	ds_read_b64_tr_b16 v[238:239], v16 offset:2048
	ds_read_b64_tr_b16 v[240:241], v16 offset:3072
	v_add_f32_e32 v252, v114, v252
	v_add_f32_e32 v252, v115, v252
	v_add_f32_e32 v252, v116, v252
	v_add_f32_e32 v252, v117, v252
	s_waitcnt lgkmcnt(8)
	v_mfma_f32_32x32x16_bf16 v[98:113], v[178:181], v[154:157], v[98:113]
	ds_read_b64_tr_b16 v[242:243], v16 offset:4096
	ds_read_b64_tr_b16 v[244:245], v16 offset:5120
	ds_read_b64_tr_b16 v[246:247], v16 offset:6144
	ds_read_b64_tr_b16 v[248:249], v16 offset:7168
	v_add_f32_e32 v252, v118, v252
	v_add_f32_e32 v252, v119, v252
	v_add_f32_e32 v252, v120, v252
	v_add_f32_e32 v252, v121, v252
	s_waitcnt lgkmcnt(11)
	v_mfma_f32_32x32x16_bf16 v[130:145], v[182:185], v[150:153], v[130:145]
	v_add_f32_e32 v252, v122, v252
	v_add_f32_e32 v252, v123, v252
	v_add_f32_e32 v252, v124, v252
	v_add_f32_e32 v252, v125, v252
	v_add_f32_e32 v252, v126, v252
	v_add_f32_e32 v252, v127, v252
	ds_read_b64_tr_b16 v[74:75], v16 offset:512
	ds_read_b64_tr_b16 v[76:77], v16 offset:1536
	ds_read_b64_tr_b16 v[78:79], v16 offset:2560
	ds_read_b64_tr_b16 v[80:81], v16 offset:3584
	s_waitcnt lgkmcnt(14)
	v_mfma_f32_32x32x16_bf16 v[98:113], v[170:173], v[150:153], v[98:113]
	v_add_f32_e32 v252, v128, v252
	v_cvt_pk_bf16_f32 v114, v114, v115
	v_cvt_pk_bf16_f32 v115, v116, v117
	v_cvt_pk_bf16_f32 v116, v118, v119
	v_cvt_pk_bf16_f32 v117, v120, v121
	v_cvt_pk_bf16_f32 v118, v122, v123
	v_cvt_pk_bf16_f32 v119, v124, v125
	v_cvt_pk_bf16_f32 v120, v126, v127
	v_cvt_pk_bf16_f32 v121, v128, v129
	v_add_f32_e32 v126, v129, v252
	v_mov_b32_e32 v127, v126
	s_waitcnt lgkmcnt(13)
	v_mfma_f32_32x32x16_bf16 v[130:145], v[66:69], v[146:149], v[130:145]
	s_cmp_ge_u32 s35, s31
	s_cbranch_scc1 .Lmla_b_noload
	s_cmp_lt_u32 s35, s30
	s_cselect_b32 s0, 0, s30
	s_cselect_b32 s1, s29, s34
	s_lshl_b32 s0, s0, 6
	s_sub_i32 s37, s1, s0
	s_lshl_b32 s1, s35, 6
	s_add_i32 s37, s37, s1
	s_lshl_b32 s0, s37, 6
	s_add_u32 s48, s44, s0
	s_addc_u32 s49, s45, 0
	s_lshl_b32 s0, s37, 11
	s_add_u32 s46, s42, s0
	s_addc_u32 s47, s43, 0
	global_load_dwordx4 v[170:173], v226, s[48:49]
	global_load_dwordx4 v[178:181], v225, s[46:47]
	global_load_dwordx4 v[182:185], v225, s[46:47] offset:128
; #define SBAR() __builtin_amdgcn_sched_barrier(0)
; __device__ __forceinline__ float psm_max(const f32x16& p0, const f32x16& p1) {
;     float pmax = p0[0];
; #pragma unroll
;     for (int r = 1; r < 16; ++r) pmax = fmaxf(pmax, p0[r]);
; #pragma unroll
;     for (int r = 0; r < 16; ++r) pmax = fmaxf(pmax, p1[r]);
;     { auto rr = __builtin_amdgcn_permlane32_swap(__float_as_uint(pmax), __float_as_uint(pmax), false, false);
;       pmax = fmaxf(__uint_as_float(rr[0]), __uint_as_float(rr[1])); }
;     return pmax;
; }
; template <bool FIRST> __device__ __forceinline__ void psm_apply(f32x16& p0, f32x16& p1, float pmax, float& m_reg, f32x16& negm, float& alpha) {
;     alpha = 1.f;
;     if (FIRST || !__builtin_expect(__all(pmax <= THR2), 1)) {
;         const float delta = FIRST ? pmax : fmaxf(pmax, 0.f);
;         if (!FIRST) alpha = __builtin_amdgcn_exp2f(-delta);
;         m_reg += delta;
; #pragma unroll
;         for (int r = 0; r < 16; ++r) { p0[r] -= delta; p1[r] -= delta; negm[r] = -m_reg; }
;     }
; #pragma unroll
;     for (int r = 0; r < 16; ++r) p0[r] = EXP_PROBE ? fmaf(p0[r], 0.001f, 1.f) : __builtin_amdgcn_exp2f(p0[r]);
; }
; template <int D0> __device__ __forceinline__ void pv_one(f32x16& od, unsigned vb, bf16x8 pa0, bf16x8 pa1, bf16x8 pa2, bf16x8 pa3) {
;     const s16x4 l0 = tr_read<v_rd_off(D0, 0, 0)>(vb), h0 = tr_read<v_rd_off(D0, 0, 1)>(vb), l1 = tr_read<v_rd_off(D0, 1, 0)>(vb), h1 = tr_read<v_rd_off(D0, 1, 1)>(vb);
;     const s16x4 l2 = tr_read<v_rd_off(D0, 2, 0)>(vb), h2 = tr_read<v_rd_off(D0, 2, 1)>(vb), l3 = tr_read<v_rd_off(D0, 3, 0)>(vb), h3 = tr_read<v_rd_off(D0, 3, 1)>(vb);
;     asm volatile("s_waitcnt lgkmcnt(0)" ::: "memory"); SBAR();
;     ...
;     od = __builtin_amdgcn_mfma_f32_32x32x16_bf16(ATT_PK(l0, h0), pa0, od, 0, 0, 0);
;     od = __builtin_amdgcn_mfma_f32_32x32x16_bf16(ATT_PK(l1, h1), pa1, od, 0, 0, 0);
;     od = __builtin_amdgcn_mfma_f32_32x32x16_bf16(ATT_PK(l2, h2), pa2, od, 0, 0, 0);
;     od = __builtin_amdgcn_mfma_f32_32x32x16_bf16(ATT_PK(l3, h3), pa3, od, 0, 0, 0);
.Lmla_b_ld_done:
	ds_read_b64_tr_b16 v[66:67], v16 offset:4608
	ds_read_b64_tr_b16 v[68:69], v16 offset:5632
	s_waitcnt lgkmcnt(14)
	v_mfma_f32_32x32x16_bf16 v[98:113], v[70:73], v[146:149], v[98:113]
	v_permlane32_swap_b32_e32 v126, v127
	ds_read_b64_tr_b16 v[70:71], v16 offset:6656
	ds_read_b64_tr_b16 v[72:73], v16 offset:7680
	s_nop 3
	v_max3_f32 v250, v130, v131, v132
	v_max3_f32 v250, v250, v133, v134
	v_max3_f32 v250, v250, v135, v136
	v_max3_f32 v250, v250, v137, v138
	v_max3_f32 v250, v250, v139, v140
	v_max3_f32 v250, v250, v141, v142
	v_max3_f32 v250, v250, v143, v144
	v_max3_f32 v250, v250, v145, v98
	v_max3_f32 v250, v250, v99, v100
	s_waitcnt lgkmcnt(8)
	v_mfma_f32_32x32x16_bf16 v[50:65], v[234:237], v[12:15], v[50:65]
	v_max3_f32 v250, v250, v101, v102
	v_max3_f32 v250, v250, v103, v104
	v_max3_f32 v250, v250, v105, v106
	v_mfma_f32_32x32x16_bf16 v[50:65], v[238:241], v[230:233], v[50:65]
	v_max3_f32 v250, v250, v107, v108
	v_max3_f32 v250, v250, v109, v110
	v_max3_f32 v250, v250, v111, v112
	v_mfma_f32_32x32x16_bf16 v[50:65], v[242:245], v[114:117], v[50:65]
	v_max_f32_e32 v250, v250, v113
	s_nop 0
	s_nop 0
	v_mfma_f32_32x32x16_bf16 v[50:65], v[246:249], v[118:121], v[50:65]
	v_mov_b32_e32 v251, v250
	s_nop 1
	v_permlane32_swap_b32_e32 v250, v251
	v_max_f32_e32 v250, v250, v251
	v_cmp_ge_f32_e32 vcc, s28, v250
	s_cmp_eq_u64 vcc, exec
	v_mov_b32_e32 v16, 1.0
	s_cbranch_scc0 .LBB0_543
.LBB0_536:
	s_waitcnt lgkmcnt(0)
	v_mfma_f32_32x32x16_bf16 v[34:49], v[74:77], v[12:15], v[34:49]
	s_waitcnt vmcnt(3)
	v_add_u32_e32 v253, s11, v187
	ds_write_b128 v253, v[8:11]
	v_add_u32_e32 v253, s11, v214
	ds_write_b128 v253, v[4:7] offset:12288
	s_cmp_eq_u64 s[2:3], 0
	s_cbranch_scc1 .Lmla_b_nokr
	v_add_u32_e32 v253, s11, v216
	ds_write_b128 v253, v[174:177] offset:8192
.Lmla_b_nokr:
	v_exp_f32_e32 v243, v130
	v_exp_f32_e32 v245, v131
	v_mfma_f32_32x32x16_bf16 v[34:49], v[78:81], v[230:233], v[34:49]
	v_exp_f32_e32 v241, v132
	v_exp_f32_e32 v244, v133
	v_exp_f32_e32 v239, v134
	v_exp_f32_e32 v242, v135
	v_mfma_f32_32x32x16_bf16 v[34:49], v[66:69], v[114:117], v[34:49]
	v_exp_f32_e32 v238, v136
	v_exp_f32_e32 v240, v137
	v_exp_f32_e32 v236, v138
	v_exp_f32_e32 v237, v139
	v_exp_f32_e32 v235, v141
	v_mfma_f32_32x32x16_bf16 v[34:49], v[70:73], v[118:121], v[34:49]
	v_exp_f32_e32 v234, v143
	v_exp_f32_e32 v233, v140
	v_exp_f32_e32 v231, v142
	v_exp_f32_e32 v230, v144
	v_exp_f32_e32 v232, v145
	v_cmp_gt_f32_e32 vcc, 1.0, v16
	s_cbranch_vccz .LBB0_540
	s_nop 7
	s_nop 7
	v_pk_mul_f32 v[64:65], v[64:65], v[16:17] op_sel_hi:[1,0]
	v_pk_mul_f32 v[62:63], v[62:63], v[16:17] op_sel_hi:[1,0]
	v_pk_mul_f32 v[60:61], v[60:61], v[16:17] op_sel_hi:[1,0]
	v_pk_mul_f32 v[58:59], v[58:59], v[16:17] op_sel_hi:[1,0]
	v_pk_mul_f32 v[56:57], v[56:57], v[16:17] op_sel_hi:[1,0]
	v_pk_mul_f32 v[54:55], v[54:55], v[16:17] op_sel_hi:[1,0]
	v_pk_mul_f32 v[52:53], v[52:53], v[16:17] op_sel_hi:[1,0]
	v_pk_mul_f32 v[50:51], v[50:51], v[16:17] op_sel_hi:[1,0]
	v_pk_mul_f32 v[48:49], v[48:49], v[16:17] op_sel_hi:[1,0]
	v_pk_mul_f32 v[46:47], v[46:47], v[16:17] op_sel_hi:[1,0]
	v_pk_mul_f32 v[44:45], v[44:45], v[16:17] op_sel_hi:[1,0]
	v_pk_mul_f32 v[42:43], v[42:43], v[16:17] op_sel_hi:[1,0]
	v_pk_mul_f32 v[40:41], v[40:41], v[16:17] op_sel_hi:[1,0]
	v_pk_mul_f32 v[38:39], v[38:39], v[16:17] op_sel_hi:[1,0]
	v_pk_mul_f32 v[36:37], v[36:37], v[16:17] op_sel_hi:[1,0]
	v_pk_mul_f32 v[34:35], v[34:35], v[16:17] op_sel_hi:[1,0]
